# speedup vs baseline: 1.0231x; 1.0067x over previous
.LBB3_10:
	v_add_u32_e32 v6, s19, v89
	v_add_u32_e32 v8, 8, v6
	v_or_b32_e32 v7, s20, v144
	v_or_b32_e32 v2, v8, v143
	v_lshl_or_b32 v4, v2, 7, v7
	s_or_b32 s0, s4, 0x8000
	v_add_u32_e32 v2, s4, v4
	v_ashrrev_i32_e32 v3, 31, v2
	v_add_u32_e32 v4, s0, v4
	v_lshlrev_b64 v[2:3], 5, v[2:3]
	v_ashrrev_i32_e32 v5, 31, v4
	v_lshl_add_u64 v[2:3], v[84:85], 0, v[2:3]
	v_lshlrev_b64 v[4:5], 5, v[4:5]
	s_lshr_b32 s1, s20, 4
	s_add_i32 s2, s7, s5
	s_add_i32 s7, s7, s6
	v_lshl_add_u64 v[4:5], v[84:85], 0, v[4:5]
	global_load_dwordx4 v[58:61], v[2:3], off
	global_load_dwordx4 v[62:65], v[4:5], off
	v_or_b32_e32 v2, v8, v95
	s_lshl_b32 s2, s2, 10
	s_lshl_b32 s3, s7, 10
	v_lshl_or_b32 v4, v2, 3, s1
	v_add_u32_e32 v2, s2, v4
	v_add_u32_e32 v4, s3, v4
	v_ashrrev_i32_e32 v3, 31, v2
	v_ashrrev_i32_e32 v5, 31, v4
	v_lshlrev_b64 v[2:3], 6, v[2:3]
	v_lshlrev_b64 v[4:5], 6, v[4:5]
	v_lshl_add_u64 v[2:3], v[86:87], 0, v[2:3]
	v_lshl_add_u64 v[4:5], v[86:87], 0, v[4:5]
	global_load_ushort v132, v[2:3], off
	global_load_ushort v133, v[4:5], off
	v_ashrrev_i32_e32 v89, 31, v88
	v_add_u32_e32 v4, 0x300, v88
	v_lshl_add_u64 v[2:3], v[88:89], 4, s[8:9]
	v_ashrrev_i32_e32 v5, 31, v4
	v_lshl_add_u64 v[4:5], v[4:5], 4, s[8:9]
	global_load_dwordx4 v[66:69], v[2:3], off
	global_load_dwordx4 v[70:73], v[4:5], off
	global_load_dword v96, v[90:91], off
	global_load_dword v98, v[90:91], off offset:1536
	v_or_b32_e32 v2, v6, v95
	v_lshl_or_b32 v4, v2, 3, s1
	v_add_u32_e32 v2, s3, v4
	v_ashrrev_i32_e32 v3, 31, v2
	v_add_u32_e32 v4, s2, v4
	v_lshlrev_b64 v[2:3], 6, v[2:3]
	v_ashrrev_i32_e32 v5, 31, v4
	v_lshl_add_u64 v[2:3], v[86:87], 0, v[2:3]
	v_lshlrev_b64 v[4:5], 6, v[4:5]
	v_lshl_add_u64 v[4:5], v[86:87], 0, v[4:5]
	global_load_ushort v138, v[2:3], off
	global_load_ushort v139, v[4:5], off
	v_or_b32_e32 v2, v6, v143
	v_lshl_or_b32 v4, v2, 7, v7
	v_add_u32_e32 v2, s0, v4
	v_ashrrev_i32_e32 v3, 31, v2
	v_add_u32_e32 v4, s4, v4
	v_lshlrev_b64 v[2:3], 5, v[2:3]
	v_ashrrev_i32_e32 v5, 31, v4
	v_lshl_add_u64 v[2:3], v[84:85], 0, v[2:3]
	v_lshlrev_b64 v[4:5], 5, v[4:5]
	v_lshl_add_u64 v[4:5], v[84:85], 0, v[4:5]
	global_load_dwordx4 v[90:93], v[2:3], off
	global_load_dwordx4 v[18:21], v[4:5], off
	v_lshl_or_b32 v134, v142, 5, v82
	v_add_u32_e32 v135, 0x8200, v83
	v_mov_b32_e32 v95, v94
	s_mov_b32 s6, 0
	s_mov_b64 s[0:1], -1
	s_mov_b32 s4, 0x7f61b1e6
	s_mov_b32 s5, 0x42800000
	s_waitcnt vmcnt(5)
	v_mov_b32_e32 v97, v96
	s_waitcnt vmcnt(4)
	v_mov_b32_e32 v99, v98
	s_branch .LBB3_12
.LBB3_11:
	v_pk_mul_f32 v[4:5], v[98:99], v[34:35]
	s_xor_b64 s[2:3], s[0:1], -1
	v_exp_f32_e32 v6, v5
	v_exp_f32_e32 v7, v4
	v_pk_mul_f32 v[4:5], v[34:35], v[18:19]
	s_nop 0
	v_fma_f32 v5, v48, v6, v5
	v_fmac_f32_e32 v4, v7, v5
	v_pk_fma_f32 v[10:11], v[2:3], v[4:5], v[100:101]
	s_cmp_lg_u32 s6, 0
	s_cbranch_scc1 .Lp3_nobar
	s_waitcnt lgkmcnt(0)
	s_barrier
.Lp3_nobar:
	v_lshl_add_u32 v6, v137, 1, v135
	ds_read_b128 v[2:5], v6
	ds_read_b128 v[6:9], v6 offset:16
	s_waitcnt lgkmcnt(1)
	v_cvt_f32_f16_e32 v12, v2
	v_cvt_f32_f16_sdwa v13, v2 dst_sel:DWORD dst_unused:UNUSED_PAD src0_sel:WORD_1
	v_cvt_f32_f16_e32 v2, v3
	v_cvt_f32_f16_sdwa v3, v3 dst_sel:DWORD dst_unused:UNUSED_PAD src0_sel:WORD_1
	v_cvt_f32_f16_e32 v14, v4
	v_pk_add_f32 v[10:11], v[10:11], v[12:13]
	v_cvt_f32_f16_sdwa v15, v4 dst_sel:DWORD dst_unused:UNUSED_PAD src0_sel:WORD_1
	v_pk_add_f32 v[2:3], v[128:129], v[2:3]
	v_cvt_f32_f16_e32 v4, v5
	v_cvt_f32_f16_sdwa v5, v5 dst_sel:DWORD dst_unused:UNUSED_PAD src0_sel:WORD_1
	v_pk_fma_f32 v[10:11], v[94:95], v[86:87], v[10:11]
	v_pk_fma_f32 v[12:13], v[94:95], v[88:89], v[2:3]
	ds_write_b128 v136, v[10:13]
	s_waitcnt lgkmcnt(1)
	v_cvt_f32_f16_e32 v10, v6
	v_cvt_f32_f16_sdwa v11, v6 dst_sel:DWORD dst_unused:UNUSED_PAD src0_sel:WORD_1
	v_cvt_f32_f16_e32 v6, v7
	v_cvt_f32_f16_sdwa v7, v7 dst_sel:DWORD dst_unused:UNUSED_PAD src0_sel:WORD_1
	v_pk_add_f32 v[2:3], v[36:37], v[14:15]
	v_pk_add_f32 v[4:5], v[38:39], v[4:5]
	v_pk_fma_f32 v[2:3], v[94:95], v[82:83], v[2:3]
	v_pk_fma_f32 v[4:5], v[94:95], v[84:85], v[4:5]
	ds_write_b128 v136, v[2:5] offset:16
	v_pk_add_f32 v[4:5], v[42:43], v[6:7]
	v_cvt_f32_f16_e32 v6, v8
	v_cvt_f32_f16_sdwa v7, v8 dst_sel:DWORD dst_unused:UNUSED_PAD src0_sel:WORD_1
	v_cvt_f32_f16_e32 v8, v9
	v_cvt_f32_f16_sdwa v9, v9 dst_sel:DWORD dst_unused:UNUSED_PAD src0_sel:WORD_1
	v_pk_add_f32 v[2:3], v[40:41], v[10:11]
	v_pk_fma_f32 v[4:5], v[94:95], v[80:81], v[4:5]
	v_pk_fma_f32 v[2:3], v[94:95], v[78:79], v[2:3]
	ds_write_b128 v136, v[2:5] offset:32
	v_pk_add_f32 v[2:3], v[44:45], v[6:7]
	v_pk_add_f32 v[4:5], v[46:47], v[8:9]
	v_pk_fma_f32 v[2:3], v[94:95], v[74:75], v[2:3]
	v_pk_fma_f32 v[4:5], v[94:95], v[76:77], v[4:5]
	ds_write_b128 v136, v[2:5] offset:48
	v_mov_b64_e32 v[92:93], v[64:65]
	v_mov_b64_e32 v[18:19], v[58:59]
	s_movk_i32 s6, 0x80
	s_mov_b64 s[0:1], 0
	s_andn2_b64 vcc, exec, s[2:3]
	v_mov_b32_e32 v138, v133
	v_mov_b32_e32 v139, v132
	v_mov_b64_e32 v[90:91], v[62:63]
	v_mov_b64_e32 v[20:21], v[60:61]
	s_cbranch_vccz .LBB3_19

.LBB3_19:
	s_lshl_b32 s0, s20, 2
	s_add_u32 s0, s14, s0
	s_addc_u32 s1, s15, 0
	s_lshl_b32 s2, s18, 7
	s_add_i32 s2, s2, s19
	s_lshl_b32 s2, s2, 9
	s_add_u32 s24, s0, s2
	s_addc_u32 s25, s1, 0
	s_add_u32 s26, s24, 0x40000
	s_addc_u32 s27, s25, 0
	s_add_u32 s28, s26, 0x40000
	s_addc_u32 s29, s27, 0
	s_add_u32 s30, s28, 0x40000
	s_addc_u32 s31, s29, 0
	s_add_u32 s32, s30, 0x40000
	s_addc_u32 s33, s31, 0
	s_add_u32 s34, s32, 0x40000
	s_addc_u32 s35, s33, 0
	s_add_u32 s36, s34, 0x40000
	s_addc_u32 s37, s35, 0
	s_add_u32 s38, s36, 0x40000
	s_addc_u32 s39, s37, 0
	v_lshrrev_b32_e32 v1, 6, v0
	v_bfe_u32 v36, v0, 2, 4
	v_lshlrev_b32_e32 v37, 4, v0
	v_and_b32_e32 v37, 48, v37
	v_lshl_add_u32 v10, v1, 7, v36
	v_lshl_add_u32 v10, v10, 9, v37
	v_mul_u32_u24_e32 v1, 0x410, v1
	v_lshl_add_u32 v36, v36, 6, v37
	v_add_u32_e32 v11, v1, v36
	s_waitcnt lgkmcnt(0)
	s_barrier
	ds_read_b128 v[2:5], v11
	ds_read_b128 v[6:9], v11 offset:4160
	ds_read_b128 v[12:15], v11 offset:8320
	ds_read_b128 v[16:19], v11 offset:12480
	ds_read_b128 v[20:23], v11 offset:16640
	ds_read_b128 v[24:27], v11 offset:20800
	ds_read_b128 v[28:31], v11 offset:24960
	ds_read_b128 v[32:35], v11 offset:29120
	s_waitcnt lgkmcnt(7)
	global_store_dwordx4 v10, v[2:5], s[24:25] nt
	s_waitcnt lgkmcnt(6)
	global_store_dwordx4 v10, v[6:9], s[26:27] nt
	s_waitcnt lgkmcnt(5)
	global_store_dwordx4 v10, v[12:15], s[28:29] nt
	s_waitcnt lgkmcnt(4)
	global_store_dwordx4 v10, v[16:19], s[30:31] nt
	s_waitcnt lgkmcnt(3)
	global_store_dwordx4 v10, v[20:23], s[32:33] nt
	s_waitcnt lgkmcnt(2)
	global_store_dwordx4 v10, v[24:27], s[34:35] nt
	s_waitcnt lgkmcnt(1)
	global_store_dwordx4 v10, v[28:31], s[36:37] nt
	s_waitcnt lgkmcnt(0)
	global_store_dwordx4 v10, v[32:35], s[38:39] nt
